# down epilogues (both layers): the 8 output stores per unit also use one v_lshl_add_u32 + SALU base pair instead of 64-bit VALU address chains
# speedup vs baseline: 1.0064x; 1.0034x over previous
.LBB0_1627:
	v_lshlrev_b32_e32 v158, 16, v6
	v_and_b32_e32 v159, 0xffff0000, v6
	v_lshlrev_b32_e32 v154, 16, v8
	v_and_b32_e32 v155, 0xffff0000, v8
	v_lshlrev_b32_e32 v156, 16, v7
	v_and_b32_e32 v157, 0xffff0000, v7
	v_lshlrev_b32_e32 v152, 16, v9
	v_and_b32_e32 v153, 0xffff0000, v9
	s_waitcnt vmcnt(10)
	v_lshlrev_b32_e32 v6, 16, v4
	v_and_b32_e32 v7, 0xffff0000, v4
	v_mul_f32_e32 v4, 0x41000000, v146
	v_pk_fma_f32 v[134:135], v[134:135], s[36:37], v[158:159] op_sel_hi:[1,0,1]
	v_pk_fma_f32 v[130:131], v[130:131], s[36:37], v[154:155] op_sel_hi:[1,0,1]
	v_pk_fma_f32 v[136:137], v[136:137], s[36:37], v[156:157] op_sel_hi:[1,0,1]
	v_pk_mul_f32 v[134:135], v[4:5], v[134:135] op_sel_hi:[0,1]
	v_pk_fma_f32 v[132:133], v[132:133], s[36:37], v[152:153] op_sel_hi:[1,0,1]
	v_pk_mul_f32 v[130:131], v[4:5], v[130:131] op_sel_hi:[0,1]
	v_lshlrev_b32_e32 v150, 16, v2
	v_and_b32_e32 v151, 0xffff0000, v2
	v_lshlrev_b32_e32 v8, 16, v3
	v_and_b32_e32 v9, 0xffff0000, v3
	v_lshlrev_b32_e32 v2, 16, v5
	v_and_b32_e32 v3, 0xffff0000, v5
	v_pk_mul_f32 v[136:137], v[4:5], v[136:137] op_sel_hi:[0,1]
	v_pk_mul_f32 v[132:133], v[4:5], v[132:133] op_sel_hi:[0,1]
	v_med3_f32 v5, v134, s70, v164
	v_med3_f32 v134, v130, s70, v164
	v_med3_f32 v135, v135, s70, v164
	v_mov_b32_e32 v130, 0
	v_cvt_pk_fp8_f32 v130, v5, v135
	v_med3_f32 v136, v136, s70, v164
	v_med3_f32 v5, v137, s70, v164
	v_pk_fma_f32 v[126:127], v[126:127], s[36:37], v[150:151] op_sel_hi:[1,0,1]
	v_pk_fma_f32 v[128:129], v[128:129], s[36:37], v[8:9] op_sel_hi:[1,0,1]
	v_pk_fma_f32 v[122:123], v[122:123], s[36:37], v[6:7] op_sel_hi:[1,0,1]
	v_pk_fma_f32 v[124:125], v[124:125], s[36:37], v[2:3] op_sel_hi:[1,0,1]
	v_cvt_pk_fp8_f32 v130, v136, v5 op_sel:[0,0,1]
	v_pk_mul_f32 v[128:129], v[4:5], v[128:129] op_sel_hi:[0,1]
	v_pk_mul_f32 v[126:127], v[4:5], v[126:127] op_sel_hi:[0,1]
	v_pk_mul_f32 v[124:125], v[4:5], v[124:125] op_sel_hi:[0,1]
	v_pk_mul_f32 v[4:5], v[4:5], v[122:123] op_sel_hi:[0,1]
	v_med3_f32 v146, v131, s70, v164
	v_mov_b32_e32 v131, 0
	v_med3_f32 v122, v126, s70, v164
	v_med3_f32 v123, v4, s70, v164
	v_med3_f32 v126, v127, s70, v164
	v_med3_f32 v127, v5, s70, v164
	v_mov_b32_e32 v4, 0
	v_mov_b32_e32 v5, 0
	v_cvt_pk_fp8_f32 v131, v134, v146
	v_cvt_pk_fp8_f32 v4, v122, v126
	v_cvt_pk_fp8_f32 v5, v123, v127
	v_mov_b32_e32 v171, v0
	v_med3_f32 v132, v132, s70, v164
	v_readfirstlane_b32 s39, v171
	s_lshr_b32 s6, s39, 6
	v_med3_f32 v133, v133, s70, v164
	v_med3_f32 v128, v128, s70, v164
	v_med3_f32 v124, v124, s70, v164
	v_med3_f32 v122, v129, s70, v164
	v_med3_f32 v123, v125, s70, v164
	s_mulk_i32 s6, 0xb00
	v_cvt_pk_fp8_f32 v131, v132, v133 op_sel:[0,0,1]
	v_cvt_pk_fp8_f32 v4, v128, v122 op_sel:[0,0,1]
	v_cvt_pk_fp8_f32 v5, v124, v123 op_sel:[0,0,1]
	s_add_i32 s6, s6, 0
	v_and_b32_e32 v172, 15, v171
	v_lshrrev_b32_e32 v123, 1, v171
	s_add_i32 s41, s6, 0x20000
	v_mul_u32_u24_e32 v122, 0x50, v172
	v_and_b32_e32 v123, 24, v123
	v_add3_u32 v122, s41, v122, v123
	s_and_b32 s7, s39, 0xc0
	ds_write2_b64 v122, v[130:131], v[4:5] offset1:4
	v_bfe_u32 v4, v171, 2, 4
	s_ashr_i32 s39, s39, 2
	v_mul_u32_u24_e32 v5, 0x50, v4
	v_lshlrev_b32_e32 v123, 4, v171
	s_andn2_b32 s39, s39, 63
	v_lshl_or_b32 v4, s48, 8, v4
	v_and_b32_e32 v146, 48, v123
	v_add_u32_e32 v4, s39, v4
	v_mul_f32_e32 v130, 0x41000000, v170
	v_pk_fma_f32 v[118:119], v[118:119], s[36:37], v[158:159] op_sel_hi:[1,0,1]
	v_pk_fma_f32 v[114:115], v[114:115], s[36:37], v[154:155] op_sel_hi:[1,0,1]
	v_add3_u32 v123, s41, v5, v146
	v_ashrrev_i32_e32 v5, 31, v4
	v_pk_mul_f32 v[118:119], v[130:131], v[118:119] op_sel_hi:[0,1]
	v_pk_mul_f32 v[114:115], v[130:131], v[114:115] op_sel_hi:[0,1]
	v_lshl_add_u32 v128, v4, 10, v146
	v_med3_f32 v5, v118, s70, v164
	v_med3_f32 v118, v114, s70, v164
	v_med3_f32 v119, v119, s70, v164
	v_mov_b32_e32 v114, v147
	v_cvt_pk_fp8_f32 v114, v5, v119
	v_pk_fma_f32 v[120:121], v[120:121], s[36:37], v[156:157] op_sel_hi:[1,0,1]
	v_pk_fma_f32 v[116:117], v[116:117], s[36:37], v[152:153] op_sel_hi:[1,0,1]
	v_pk_mul_f32 v[120:121], v[130:131], v[120:121] op_sel_hi:[0,1]
	v_pk_mul_f32 v[116:117], v[130:131], v[116:117] op_sel_hi:[0,1]
	v_med3_f32 v131, v115, s70, v164
	v_pk_fma_f32 v[110:111], v[110:111], s[36:37], v[150:151] op_sel_hi:[1,0,1]
	v_pk_fma_f32 v[106:107], v[106:107], s[36:37], v[6:7] op_sel_hi:[1,0,1]
	v_med3_f32 v120, v120, s70, v164
	v_med3_f32 v5, v121, s70, v164
	v_pk_mul_f32 v[110:111], v[130:131], v[110:111] op_sel_hi:[0,1]
	v_pk_mul_f32 v[106:107], v[130:131], v[106:107] op_sel_hi:[0,1]
	v_cvt_pk_fp8_f32 v114, v120, v5 op_sel:[0,0,1]
	v_med3_f32 v5, v110, s70, v164
	v_med3_f32 v110, v106, s70, v164
	v_med3_f32 v111, v111, s70, v164
	v_mov_b32_e32 v106, v147
	v_cvt_pk_fp8_f32 v106, v5, v111
	v_pk_fma_f32 v[112:113], v[112:113], s[36:37], v[8:9] op_sel_hi:[1,0,1]
	v_mov_b32_e32 v115, v147
	v_pk_mul_f32 v[112:113], v[130:131], v[112:113] op_sel_hi:[0,1]
	v_med3_f32 v112, v112, s70, v164
	v_med3_f32 v5, v113, s70, v164
	v_cvt_pk_fp8_f32 v106, v112, v5 op_sel:[0,0,1]
	v_mul_f32_e32 v112, 0x41000000, v169
	v_pk_fma_f32 v[102:103], v[102:103], s[36:37], v[158:159] op_sel_hi:[1,0,1]
	v_pk_fma_f32 v[98:99], v[98:99], s[36:37], v[154:155] op_sel_hi:[1,0,1]
	v_cvt_pk_fp8_f32 v115, v118, v131
	v_pk_mul_f32 v[102:103], v[112:113], v[102:103] op_sel_hi:[0,1]
	v_pk_mul_f32 v[98:99], v[112:113], v[98:99] op_sel_hi:[0,1]
	v_med3_f32 v5, v102, s70, v164
	v_med3_f32 v102, v98, s70, v164
	v_med3_f32 v103, v103, s70, v164
	v_mov_b32_e32 v98, v147
	v_cvt_pk_fp8_f32 v98, v5, v103
	v_med3_f32 v116, v116, s70, v164
	v_med3_f32 v117, v117, s70, v164
	v_pk_fma_f32 v[104:105], v[104:105], s[36:37], v[156:157] op_sel_hi:[1,0,1]
	v_pk_fma_f32 v[100:101], v[100:101], s[36:37], v[152:153] op_sel_hi:[1,0,1]
	v_cvt_pk_fp8_f32 v115, v116, v117 op_sel:[0,0,1]
	v_med3_f32 v116, v107, s70, v164
	v_mov_b32_e32 v107, v147
	v_pk_mul_f32 v[104:105], v[112:113], v[104:105] op_sel_hi:[0,1]
	v_pk_mul_f32 v[100:101], v[112:113], v[100:101] op_sel_hi:[0,1]
	v_med3_f32 v113, v99, s70, v164
	v_pk_fma_f32 v[94:95], v[94:95], s[36:37], v[150:151] op_sel_hi:[1,0,1]
	v_pk_fma_f32 v[90:91], v[90:91], s[36:37], v[6:7] op_sel_hi:[1,0,1]
	v_cvt_pk_fp8_f32 v107, v110, v116
	v_med3_f32 v104, v104, s70, v164
	v_med3_f32 v5, v105, s70, v164
	v_pk_mul_f32 v[94:95], v[112:113], v[94:95] op_sel_hi:[0,1]
	v_pk_mul_f32 v[90:91], v[112:113], v[90:91] op_sel_hi:[0,1]
	v_pk_fma_f32 v[108:109], v[108:109], s[36:37], v[2:3] op_sel_hi:[1,0,1]
	v_mov_b32_e32 v99, v147
	v_cvt_pk_fp8_f32 v98, v104, v5 op_sel:[0,0,1]
	v_med3_f32 v5, v94, s70, v164
	v_med3_f32 v94, v90, s70, v164
	v_med3_f32 v95, v95, s70, v164
	v_mov_b32_e32 v90, v147
	s_lshl_b32 s6, s50, 8
	ds_read_b128 v[124:127], v123
	v_pk_mul_f32 v[108:109], v[130:131], v[108:109] op_sel_hi:[0,1]
	v_cvt_pk_fp8_f32 v99, v102, v113
	v_cvt_pk_fp8_f32 v90, v5, v95
	s_or_b32 s6, s7, s6
	v_med3_f32 v108, v108, s70, v164
	v_med3_f32 v109, v109, s70, v164
	v_pk_fma_f32 v[96:97], v[96:97], s[36:37], v[8:9] op_sel_hi:[1,0,1]
	s_ashr_i32 s7, s6, 31
	v_cvt_pk_fp8_f32 v107, v108, v109 op_sel:[0,0,1]
	v_pk_mul_f32 v[96:97], v[112:113], v[96:97] op_sel_hi:[0,1]
	s_add_u32 s86, s16, s6
	s_addc_u32 s87, s17, s7
	v_med3_f32 v100, v100, s70, v164
	v_med3_f32 v101, v101, s70, v164
	v_med3_f32 v96, v96, s70, v164
	v_med3_f32 v5, v97, s70, v164
	v_mov_b32_e32 v108, v128
	v_cvt_pk_fp8_f32 v99, v100, v101 op_sel:[0,0,1]
	v_med3_f32 v100, v91, s70, v164
	v_mov_b32_e32 v91, v147
	v_cvt_pk_fp8_f32 v90, v96, v5 op_sel:[0,0,1]
	v_mul_f32_e32 v96, 0x41000000, v168
	v_pk_fma_f32 v[78:79], v[78:79], s[36:37], v[158:159] op_sel_hi:[1,0,1]
	v_pk_fma_f32 v[74:75], v[74:75], s[36:37], v[154:155] op_sel_hi:[1,0,1]
	s_waitcnt lgkmcnt(0)
	global_store_dwordx4 v108, v[124:127], s[86:87]
	v_cvt_pk_fp8_f32 v91, v94, v100
	v_pk_fma_f32 v[80:81], v[80:81], s[36:37], v[156:157] op_sel_hi:[1,0,1]
	v_pk_mul_f32 v[78:79], v[96:97], v[78:79] op_sel_hi:[0,1]
	v_pk_fma_f32 v[76:77], v[76:77], s[36:37], v[152:153] op_sel_hi:[1,0,1]
	v_pk_mul_f32 v[74:75], v[96:97], v[74:75] op_sel_hi:[0,1]
	ds_write2_b64 v122, v[114:115], v[106:107] offset1:4
	v_or_b32_e32 v110, 16, v4
	v_pk_fma_f32 v[92:93], v[92:93], s[36:37], v[2:3] op_sel_hi:[1,0,1]
	v_pk_mul_f32 v[80:81], v[96:97], v[80:81] op_sel_hi:[0,1]
	v_pk_mul_f32 v[76:77], v[96:97], v[76:77] op_sel_hi:[0,1]
	v_med3_f32 v5, v78, s70, v164
	v_med3_f32 v78, v74, s70, v164
	v_med3_f32 v79, v79, s70, v164
	v_med3_f32 v97, v75, s70, v164
	v_mov_b32_e32 v74, v147
	v_mov_b32_e32 v75, v147
	ds_read_b128 v[106:109], v123
	v_ashrrev_i32_e32 v111, 31, v110
	v_pk_mul_f32 v[92:93], v[112:113], v[92:93] op_sel_hi:[0,1]
	v_cvt_pk_fp8_f32 v74, v5, v79
	v_cvt_pk_fp8_f32 v75, v78, v97
	v_lshl_add_u32 v110, v110, 10, v146
	v_med3_f32 v92, v92, s70, v164
	v_med3_f32 v93, v93, s70, v164
	v_cvt_pk_fp8_f32 v91, v92, v93 op_sel:[0,0,1]
	v_pk_fma_f32 v[62:63], v[62:63], s[36:37], v[150:151] op_sel_hi:[1,0,1]
	v_pk_fma_f32 v[58:59], v[58:59], s[36:37], v[6:7] op_sel_hi:[1,0,1]
	s_add_u32 s86, s16, s6
	s_addc_u32 s87, s17, s7
	v_med3_f32 v80, v80, s70, v164
	v_med3_f32 v76, v76, s70, v164
	v_med3_f32 v5, v81, s70, v164
	v_med3_f32 v77, v77, s70, v164
	v_pk_mul_f32 v[62:63], v[96:97], v[62:63] op_sel_hi:[0,1]
	v_pk_mul_f32 v[58:59], v[96:97], v[58:59] op_sel_hi:[0,1]
	v_mov_b32_e32 v92, v110
	v_cvt_pk_fp8_f32 v74, v80, v5 op_sel:[0,0,1]
	v_cvt_pk_fp8_f32 v75, v76, v77 op_sel:[0,0,1]
	v_med3_f32 v5, v62, s70, v164
	v_med3_f32 v62, v58, s70, v164
	v_med3_f32 v63, v63, s70, v164
	v_med3_f32 v76, v59, s70, v164
	v_mov_b32_e32 v58, v147
	v_mov_b32_e32 v59, v147
	s_waitcnt lgkmcnt(0)
	global_store_dwordx4 v92, v[106:109], s[86:87]
	v_cvt_pk_fp8_f32 v58, v5, v63
	v_cvt_pk_fp8_f32 v59, v62, v76
	ds_write2_b64 v122, v[98:99], v[90:91] offset1:4
	v_or_b32_e32 v94, 32, v4
	v_pk_fma_f32 v[64:65], v[64:65], s[36:37], v[8:9] op_sel_hi:[1,0,1]
	v_pk_fma_f32 v[60:61], v[60:61], s[36:37], v[2:3] op_sel_hi:[1,0,1]
	ds_read_b128 v[90:93], v123
	v_ashrrev_i32_e32 v95, 31, v94
	v_pk_mul_f32 v[64:65], v[96:97], v[64:65] op_sel_hi:[0,1]
	v_pk_mul_f32 v[60:61], v[96:97], v[60:61] op_sel_hi:[0,1]
	v_lshl_add_u32 v94, v94, 10, v146
	v_med3_f32 v64, v64, s70, v164
	v_med3_f32 v60, v60, s70, v164
	v_med3_f32 v5, v65, s70, v164
	v_med3_f32 v61, v61, s70, v164
	v_cvt_pk_fp8_f32 v58, v64, v5 op_sel:[0,0,1]
	v_cvt_pk_fp8_f32 v59, v60, v61 op_sel:[0,0,1]
	s_add_u32 s86, s16, s6
	s_addc_u32 s87, s17, s7
	v_mov_b32_e32 v60, v94
	s_waitcnt lgkmcnt(0)
	global_store_dwordx4 v60, v[90:93], s[86:87]
	ds_write2_b64 v122, v[74:75], v[58:59] offset1:4
	v_mul_f32_e32 v64, 0x41000000, v167
	v_pk_fma_f32 v[74:75], v[86:87], s[36:37], v[158:159] op_sel_hi:[1,0,1]
	v_pk_fma_f32 v[78:79], v[82:83], s[36:37], v[154:155] op_sel_hi:[1,0,1]
	v_pk_mul_f32 v[74:75], v[64:65], v[74:75] op_sel_hi:[0,1]
	v_pk_fma_f32 v[76:77], v[88:89], s[36:37], v[156:157] op_sel_hi:[1,0,1]
	v_pk_fma_f32 v[80:81], v[84:85], s[36:37], v[152:153] op_sel_hi:[1,0,1]
	v_pk_mul_f32 v[78:79], v[64:65], v[78:79] op_sel_hi:[0,1]
	v_med3_f32 v5, v74, s70, v164
	v_med3_f32 v75, v75, s70, v164
	v_mov_b32_e32 v74, v147
	v_pk_mul_f32 v[76:77], v[64:65], v[76:77] op_sel_hi:[0,1]
	v_pk_mul_f32 v[80:81], v[64:65], v[80:81] op_sel_hi:[0,1]
	v_med3_f32 v65, v78, s70, v164
	v_med3_f32 v78, v79, s70, v164
	v_cvt_pk_fp8_f32 v74, v5, v75
	v_mov_b32_e32 v75, v147
	v_cvt_pk_fp8_f32 v75, v65, v78
	v_med3_f32 v79, v80, s70, v164
	v_med3_f32 v65, v81, s70, v164
	v_pk_fma_f32 v[70:71], v[70:71], s[36:37], v[150:151] op_sel_hi:[1,0,1]
	v_pk_fma_f32 v[72:73], v[72:73], s[36:37], v[8:9] op_sel_hi:[1,0,1]
	v_pk_fma_f32 v[66:67], v[66:67], s[36:37], v[6:7] op_sel_hi:[1,0,1]
	v_pk_fma_f32 v[68:69], v[68:69], s[36:37], v[2:3] op_sel_hi:[1,0,1]
	v_med3_f32 v76, v76, s70, v164
	v_med3_f32 v5, v77, s70, v164
	v_cvt_pk_fp8_f32 v75, v79, v65 op_sel:[0,0,1]
	v_pk_mul_f32 v[72:73], v[64:65], v[72:73] op_sel_hi:[0,1]
	v_pk_mul_f32 v[70:71], v[64:65], v[70:71] op_sel_hi:[0,1]
	v_pk_mul_f32 v[68:69], v[64:65], v[68:69] op_sel_hi:[0,1]
	v_pk_mul_f32 v[64:65], v[64:65], v[66:67] op_sel_hi:[0,1]
	v_cvt_pk_fp8_f32 v74, v76, v5 op_sel:[0,0,1]
	v_med3_f32 v5, v70, s70, v164
	v_med3_f32 v66, v64, s70, v164
	v_med3_f32 v67, v71, s70, v164
	v_med3_f32 v70, v65, s70, v164
	v_mov_b32_e32 v64, v147
	v_mov_b32_e32 v65, v147
	v_cvt_pk_fp8_f32 v64, v5, v67
	v_cvt_pk_fp8_f32 v65, v66, v70
	v_or_b32_e32 v62, 48, v4
	ds_read_b128 v[58:61], v123
	v_ashrrev_i32_e32 v63, 31, v62
	v_lshl_add_u32 v62, v62, 10, v146
	v_med3_f32 v71, v72, s70, v164
	v_med3_f32 v68, v68, s70, v164
	v_med3_f32 v5, v73, s70, v164
	v_med3_f32 v66, v69, s70, v164
	v_cvt_pk_fp8_f32 v64, v71, v5 op_sel:[0,0,1]
	v_cvt_pk_fp8_f32 v65, v68, v66 op_sel:[0,0,1]
	s_add_u32 s86, s16, s6
	s_addc_u32 s87, s17, s7
	s_waitcnt lgkmcnt(0)
	global_store_dwordx4 v62, v[58:61], s[86:87]
	ds_write2_b64 v122, v[74:75], v[64:65] offset1:4
	v_mul_f32_e32 v64, 0x41000000, v166
	v_pk_fma_f32 v[54:55], v[54:55], s[36:37], v[158:159] op_sel_hi:[1,0,1]
	v_pk_fma_f32 v[50:51], v[50:51], s[36:37], v[154:155] op_sel_hi:[1,0,1]
	v_pk_mul_f32 v[54:55], v[64:65], v[54:55] op_sel_hi:[0,1]
	v_pk_mul_f32 v[50:51], v[64:65], v[50:51] op_sel_hi:[0,1]
	v_med3_f32 v5, v54, s70, v164
	v_med3_f32 v54, v50, s70, v164
	v_med3_f32 v55, v55, s70, v164
	v_mov_b32_e32 v50, v147
	v_cvt_pk_fp8_f32 v50, v5, v55
	v_pk_fma_f32 v[56:57], v[56:57], s[36:37], v[156:157] op_sel_hi:[1,0,1]
	v_pk_fma_f32 v[52:53], v[52:53], s[36:37], v[152:153] op_sel_hi:[1,0,1]
	v_pk_mul_f32 v[56:57], v[64:65], v[56:57] op_sel_hi:[0,1]
	v_pk_mul_f32 v[52:53], v[64:65], v[52:53] op_sel_hi:[0,1]
	v_med3_f32 v65, v51, s70, v164
	v_pk_fma_f32 v[46:47], v[46:47], s[36:37], v[150:151] op_sel_hi:[1,0,1]
	v_pk_fma_f32 v[42:43], v[42:43], s[36:37], v[6:7] op_sel_hi:[1,0,1]
	v_med3_f32 v56, v56, s70, v164
	v_med3_f32 v5, v57, s70, v164
	v_pk_mul_f32 v[46:47], v[64:65], v[46:47] op_sel_hi:[0,1]
	v_pk_mul_f32 v[42:43], v[64:65], v[42:43] op_sel_hi:[0,1]
	v_cvt_pk_fp8_f32 v50, v56, v5 op_sel:[0,0,1]
	v_med3_f32 v5, v46, s70, v164
	v_med3_f32 v46, v42, s70, v164
	v_med3_f32 v47, v47, s70, v164
	v_mov_b32_e32 v42, v147
	v_cvt_pk_fp8_f32 v42, v5, v47
	v_pk_fma_f32 v[48:49], v[48:49], s[36:37], v[8:9] op_sel_hi:[1,0,1]
	v_mov_b32_e32 v51, v147
	v_pk_mul_f32 v[48:49], v[64:65], v[48:49] op_sel_hi:[0,1]
	v_med3_f32 v48, v48, s70, v164
	v_med3_f32 v5, v49, s70, v164
	v_cvt_pk_fp8_f32 v42, v48, v5 op_sel:[0,0,1]
	v_mul_f32_e32 v48, 0x41000000, v165
	v_pk_fma_f32 v[38:39], v[38:39], s[36:37], v[158:159] op_sel_hi:[1,0,1]
	v_pk_fma_f32 v[34:35], v[34:35], s[36:37], v[154:155] op_sel_hi:[1,0,1]
	v_cvt_pk_fp8_f32 v51, v54, v65
	v_pk_mul_f32 v[38:39], v[48:49], v[38:39] op_sel_hi:[0,1]
	v_pk_mul_f32 v[34:35], v[48:49], v[34:35] op_sel_hi:[0,1]
	v_med3_f32 v5, v38, s70, v164
	v_med3_f32 v38, v34, s70, v164
	v_med3_f32 v39, v39, s70, v164
	v_mov_b32_e32 v34, v147
	v_cvt_pk_fp8_f32 v34, v5, v39
	v_med3_f32 v52, v52, s70, v164
	v_med3_f32 v53, v53, s70, v164
	v_pk_fma_f32 v[40:41], v[40:41], s[36:37], v[156:157] op_sel_hi:[1,0,1]
	v_pk_fma_f32 v[36:37], v[36:37], s[36:37], v[152:153] op_sel_hi:[1,0,1]
	v_cvt_pk_fp8_f32 v51, v52, v53 op_sel:[0,0,1]
	v_med3_f32 v52, v43, s70, v164
	v_mov_b32_e32 v43, v147
	v_pk_mul_f32 v[40:41], v[48:49], v[40:41] op_sel_hi:[0,1]
	v_pk_mul_f32 v[36:37], v[48:49], v[36:37] op_sel_hi:[0,1]
	v_med3_f32 v49, v35, s70, v164
	v_pk_fma_f32 v[30:31], v[30:31], s[36:37], v[150:151] op_sel_hi:[1,0,1]
	v_pk_fma_f32 v[26:27], v[26:27], s[36:37], v[6:7] op_sel_hi:[1,0,1]
	v_cvt_pk_fp8_f32 v43, v46, v52
	v_med3_f32 v40, v40, s70, v164
	v_med3_f32 v5, v41, s70, v164
	v_pk_mul_f32 v[30:31], v[48:49], v[30:31] op_sel_hi:[0,1]
	v_pk_mul_f32 v[26:27], v[48:49], v[26:27] op_sel_hi:[0,1]
	v_add_u32_e32 v62, 0x80, v4
	v_pk_fma_f32 v[44:45], v[44:45], s[36:37], v[2:3] op_sel_hi:[1,0,1]
	v_mov_b32_e32 v35, v147
	v_cvt_pk_fp8_f32 v34, v40, v5 op_sel:[0,0,1]
	v_med3_f32 v5, v30, s70, v164
	v_med3_f32 v30, v26, s70, v164
	v_med3_f32 v31, v31, s70, v164
	v_mov_b32_e32 v26, v147
	ds_read_b128 v[58:61], v123
	v_ashrrev_i32_e32 v63, 31, v62
	v_pk_mul_f32 v[44:45], v[64:65], v[44:45] op_sel_hi:[0,1]
	v_cvt_pk_fp8_f32 v35, v38, v49
	v_cvt_pk_fp8_f32 v26, v5, v31
	v_lshl_add_u32 v62, v62, 10, v146
	v_med3_f32 v44, v44, s70, v164
	v_med3_f32 v45, v45, s70, v164
	v_pk_fma_f32 v[32:33], v[32:33], s[36:37], v[8:9] op_sel_hi:[1,0,1]
	v_cvt_pk_fp8_f32 v43, v44, v45 op_sel:[0,0,1]
	v_pk_mul_f32 v[32:33], v[48:49], v[32:33] op_sel_hi:[0,1]
	s_add_u32 s86, s16, s6
	s_addc_u32 s87, s17, s7
	v_med3_f32 v36, v36, s70, v164
	v_med3_f32 v37, v37, s70, v164
	v_med3_f32 v32, v32, s70, v164
	v_med3_f32 v5, v33, s70, v164
	v_mov_b32_e32 v44, v62
	v_cvt_pk_fp8_f32 v35, v36, v37 op_sel:[0,0,1]
	v_med3_f32 v36, v27, s70, v164
	v_mov_b32_e32 v27, v147
	v_cvt_pk_fp8_f32 v26, v32, v5 op_sel:[0,0,1]
	v_mul_f32_e32 v32, 0x41000000, v1
	v_pk_fma_f32 v[22:23], v[22:23], s[36:37], v[158:159] op_sel_hi:[1,0,1]
	v_pk_fma_f32 v[18:19], v[18:19], s[36:37], v[154:155] op_sel_hi:[1,0,1]
	s_waitcnt lgkmcnt(0)
	global_store_dwordx4 v44, v[58:61], s[86:87]
	v_cvt_pk_fp8_f32 v27, v30, v36
	v_pk_mul_f32 v[22:23], v[32:33], v[22:23] op_sel_hi:[0,1]
	v_pk_mul_f32 v[18:19], v[32:33], v[18:19] op_sel_hi:[0,1]
	ds_write2_b64 v122, v[50:51], v[42:43] offset1:4
	v_add_u32_e32 v46, 0x90, v4
	v_pk_fma_f32 v[28:29], v[28:29], s[36:37], v[2:3] op_sel_hi:[1,0,1]
	v_med3_f32 v1, v22, s70, v164
	v_med3_f32 v5, v18, s70, v164
	v_med3_f32 v22, v23, s70, v164
	v_med3_f32 v23, v19, s70, v164
	v_mov_b32_e32 v18, v147
	v_mov_b32_e32 v19, v147
	ds_read_b128 v[42:45], v123
	v_ashrrev_i32_e32 v47, 31, v46
	v_pk_mul_f32 v[28:29], v[48:49], v[28:29] op_sel_hi:[0,1]
	v_cvt_pk_fp8_f32 v18, v1, v22
	v_cvt_pk_fp8_f32 v19, v5, v23
	v_lshl_add_u32 v46, v46, 10, v146
	v_med3_f32 v28, v28, s70, v164
	v_med3_f32 v29, v29, s70, v164
	v_pk_fma_f32 v[24:25], v[24:25], s[36:37], v[156:157] op_sel_hi:[1,0,1]
	v_pk_fma_f32 v[20:21], v[20:21], s[36:37], v[152:153] op_sel_hi:[1,0,1]
	v_cvt_pk_fp8_f32 v27, v28, v29 op_sel:[0,0,1]
	v_pk_mul_f32 v[24:25], v[32:33], v[24:25] op_sel_hi:[0,1]
	v_pk_mul_f32 v[20:21], v[32:33], v[20:21] op_sel_hi:[0,1]
	v_pk_fma_f32 v[14:15], v[14:15], s[36:37], v[150:151] op_sel_hi:[1,0,1]
	v_pk_fma_f32 v[6:7], v[10:11], s[36:37], v[6:7] op_sel_hi:[1,0,1]
	s_add_u32 s86, s16, s6
	s_addc_u32 s87, s17, s7
	v_med3_f32 v24, v24, s70, v164
	v_med3_f32 v20, v20, s70, v164
	v_med3_f32 v1, v25, s70, v164
	v_med3_f32 v5, v21, s70, v164
	v_pk_mul_f32 v[14:15], v[32:33], v[14:15] op_sel_hi:[0,1]
	v_pk_mul_f32 v[6:7], v[32:33], v[6:7] op_sel_hi:[0,1]
	v_mov_b32_e32 v28, v46
	v_cvt_pk_fp8_f32 v18, v24, v1 op_sel:[0,0,1]
	v_cvt_pk_fp8_f32 v19, v20, v5 op_sel:[0,0,1]
	v_med3_f32 v1, v14, s70, v164
	v_med3_f32 v5, v6, s70, v164
	v_med3_f32 v10, v15, s70, v164
	v_med3_f32 v11, v7, s70, v164
	v_mov_b32_e32 v6, v147
	v_mov_b32_e32 v7, v147
	s_waitcnt lgkmcnt(0)
	global_store_dwordx4 v28, v[42:45], s[86:87]
	v_cvt_pk_fp8_f32 v6, v1, v10
	v_cvt_pk_fp8_f32 v7, v5, v11
	ds_write2_b64 v122, v[34:35], v[26:27] offset1:4
	v_add_u32_e32 v30, 0xa0, v4
	v_pk_fma_f32 v[8:9], v[16:17], s[36:37], v[8:9] op_sel_hi:[1,0,1]
	v_pk_fma_f32 v[2:3], v[12:13], s[36:37], v[2:3] op_sel_hi:[1,0,1]
	ds_read_b128 v[26:29], v123
	v_ashrrev_i32_e32 v31, 31, v30
	v_pk_mul_f32 v[8:9], v[32:33], v[8:9] op_sel_hi:[0,1]
	v_pk_mul_f32 v[2:3], v[32:33], v[2:3] op_sel_hi:[0,1]
	v_lshl_add_u32 v30, v30, 10, v146
	v_med3_f32 v8, v8, s70, v164
	v_med3_f32 v2, v2, s70, v164
	v_med3_f32 v1, v9, s70, v164
	v_med3_f32 v3, v3, s70, v164
	v_cvt_pk_fp8_f32 v6, v8, v1 op_sel:[0,0,1]
	v_cvt_pk_fp8_f32 v7, v2, v3 op_sel:[0,0,1]
	s_add_u32 s86, s16, s6
	s_addc_u32 s87, s17, s7
	v_mov_b32_e32 v2, v30
	s_waitcnt lgkmcnt(0)
	global_store_dwordx4 v2, v[26:29], s[86:87]
	ds_write2_b64 v122, v[18:19], v[6:7] offset1:4
	v_add_u32_e32 v2, 0xb0, v4
	ds_read_b128 v[6:9], v123
	v_ashrrev_i32_e32 v3, 31, v2
	v_lshl_add_u32 v2, v2, 10, v146
	s_add_u32 s86, s16, s6
	s_addc_u32 s87, s17, s7
	s_waitcnt lgkmcnt(0)
	global_store_dwordx4 v2, v[6:9], s[86:87]
	s_and_b64 vcc, exec, s[8:9]
	s_mov_b64 s[6:7], -1
	s_cbranch_vccnz .LBB0_1616
	v_mov_b32_e32 v12, v0
	s_lshl_b32 s7, s40, 8
	v_readfirstlane_b32 s6, v12
	s_and_b32 s8, s6, 0xc0
	s_ashr_i32 s6, s6, 2
	s_andn2_b32 s6, s6, 63
	s_add_i32 s6, s6, s7
	v_and_or_b32 v2, v12, 15, s6
	v_lshlrev_b32_e32 v4, 2, v2
	s_lshl_b64 s[6:7], s[42:43], 11
	s_add_u32 s9, s56, s6
	s_addc_u32 s39, s57, s7
	s_lshl_b32 s6, s38, 8
	global_load_dword v146, v4, s[12:13] offset:0
	global_load_dword v170, v4, s[12:13] offset:64
	global_load_dword v169, v4, s[12:13] offset:128
	global_load_dword v168, v4, s[12:13] offset:192
	global_load_dword v167, v4, s[12:13] offset:512
	global_load_dword v166, v4, s[12:13] offset:576
	global_load_dword v165, v4, s[12:13] offset:640
	global_load_dword v1, v4, s[12:13] offset:704
	s_ashr_i32 s7, s6, 31
	s_lshl_b64 s[6:7], s[6:7], 1
	s_add_u32 s6, s9, s6
	s_addc_u32 s7, s39, s7
	s_lshl_b32 s8, s8, 1
	s_add_u32 s6, s6, s8
	s_addc_u32 s7, s7, 0
	v_and_b32_e32 v2, 48, v12
	global_load_dwordx4 v[6:9], v2, s[6:7]
	s_nop 0
	global_load_dwordx4 v[2:5], v2, s[6:7] offset:64
	s_andn2_b64 vcc, exec, s[14:15]
	s_cbranch_vccnz .LBB0_1615
	s_barrier
	s_branch .LBB0_1615

.LBB0_3429:
	v_lshlrev_b32_e32 v158, 16, v6
	v_and_b32_e32 v159, 0xffff0000, v6
	v_lshlrev_b32_e32 v154, 16, v8
	v_and_b32_e32 v155, 0xffff0000, v8
	v_lshlrev_b32_e32 v156, 16, v7
	v_and_b32_e32 v157, 0xffff0000, v7
	v_lshlrev_b32_e32 v152, 16, v9
	v_and_b32_e32 v153, 0xffff0000, v9
	s_waitcnt vmcnt(10)
	v_lshlrev_b32_e32 v6, 16, v4
	v_and_b32_e32 v7, 0xffff0000, v4
	v_mul_f32_e32 v4, 0x41000000, v146
	v_pk_fma_f32 v[134:135], v[134:135], s[38:39], v[158:159] op_sel_hi:[1,0,1]
	v_pk_fma_f32 v[130:131], v[130:131], s[38:39], v[154:155] op_sel_hi:[1,0,1]
	v_pk_fma_f32 v[136:137], v[136:137], s[38:39], v[156:157] op_sel_hi:[1,0,1]
	v_pk_mul_f32 v[134:135], v[4:5], v[134:135] op_sel_hi:[0,1]
	v_pk_fma_f32 v[132:133], v[132:133], s[38:39], v[152:153] op_sel_hi:[1,0,1]
	v_pk_mul_f32 v[130:131], v[4:5], v[130:131] op_sel_hi:[0,1]
	v_lshlrev_b32_e32 v150, 16, v2
	v_and_b32_e32 v151, 0xffff0000, v2
	v_lshlrev_b32_e32 v8, 16, v3
	v_and_b32_e32 v9, 0xffff0000, v3
	v_lshlrev_b32_e32 v2, 16, v5
	v_and_b32_e32 v3, 0xffff0000, v5
	v_pk_mul_f32 v[136:137], v[4:5], v[136:137] op_sel_hi:[0,1]
	v_pk_mul_f32 v[132:133], v[4:5], v[132:133] op_sel_hi:[0,1]
	v_med3_f32 v5, v134, s75, v164
	v_med3_f32 v134, v130, s75, v164
	v_med3_f32 v135, v135, s75, v164
	v_mov_b32_e32 v130, 0
	v_cvt_pk_fp8_f32 v130, v5, v135
	v_med3_f32 v136, v136, s75, v164
	v_med3_f32 v5, v137, s75, v164
	v_pk_fma_f32 v[126:127], v[126:127], s[38:39], v[150:151] op_sel_hi:[1,0,1]
	v_pk_fma_f32 v[128:129], v[128:129], s[38:39], v[8:9] op_sel_hi:[1,0,1]
	v_pk_fma_f32 v[122:123], v[122:123], s[38:39], v[6:7] op_sel_hi:[1,0,1]
	v_pk_fma_f32 v[124:125], v[124:125], s[38:39], v[2:3] op_sel_hi:[1,0,1]
	v_cvt_pk_fp8_f32 v130, v136, v5 op_sel:[0,0,1]
	v_pk_mul_f32 v[128:129], v[4:5], v[128:129] op_sel_hi:[0,1]
	v_pk_mul_f32 v[126:127], v[4:5], v[126:127] op_sel_hi:[0,1]
	v_pk_mul_f32 v[124:125], v[4:5], v[124:125] op_sel_hi:[0,1]
	v_pk_mul_f32 v[4:5], v[4:5], v[122:123] op_sel_hi:[0,1]
	v_med3_f32 v146, v131, s75, v164
	v_mov_b32_e32 v131, 0
	v_med3_f32 v122, v126, s75, v164
	v_med3_f32 v123, v4, s75, v164
	v_med3_f32 v126, v127, s75, v164
	v_med3_f32 v127, v5, s75, v164
	v_mov_b32_e32 v4, 0
	v_mov_b32_e32 v5, 0
	v_cvt_pk_fp8_f32 v131, v134, v146
	v_cvt_pk_fp8_f32 v4, v122, v126
	v_cvt_pk_fp8_f32 v5, v123, v127
	v_mov_b32_e32 v171, v0
	v_med3_f32 v132, v132, s75, v164
	v_readfirstlane_b32 s41, v171
	s_lshr_b32 s8, s41, 6
	v_med3_f32 v133, v133, s75, v164
	v_med3_f32 v128, v128, s75, v164
	v_med3_f32 v124, v124, s75, v164
	v_med3_f32 v122, v129, s75, v164
	v_med3_f32 v123, v125, s75, v164
	s_mulk_i32 s8, 0xb00
	v_cvt_pk_fp8_f32 v131, v132, v133 op_sel:[0,0,1]
	v_cvt_pk_fp8_f32 v4, v128, v122 op_sel:[0,0,1]
	v_cvt_pk_fp8_f32 v5, v124, v123 op_sel:[0,0,1]
	s_add_i32 s8, s8, 0
	v_and_b32_e32 v172, 15, v171
	v_lshrrev_b32_e32 v123, 1, v171
	s_add_i32 s43, s8, 0x20000
	v_mul_u32_u24_e32 v122, 0x50, v172
	v_and_b32_e32 v123, 24, v123
	v_add3_u32 v122, s43, v122, v123
	s_and_b32 s9, s41, 0xc0
	ds_write2_b64 v122, v[130:131], v[4:5] offset1:4
	v_bfe_u32 v4, v171, 2, 4
	s_ashr_i32 s41, s41, 2
	v_mul_u32_u24_e32 v5, 0x50, v4
	v_lshlrev_b32_e32 v123, 4, v171
	s_andn2_b32 s41, s41, 63
	v_lshl_or_b32 v4, s50, 8, v4
	v_and_b32_e32 v146, 48, v123
	v_add_u32_e32 v4, s41, v4
	v_mul_f32_e32 v130, 0x41000000, v170
	v_pk_fma_f32 v[118:119], v[118:119], s[38:39], v[158:159] op_sel_hi:[1,0,1]
	v_pk_fma_f32 v[114:115], v[114:115], s[38:39], v[154:155] op_sel_hi:[1,0,1]
	v_add3_u32 v123, s43, v5, v146
	v_ashrrev_i32_e32 v5, 31, v4
	v_pk_mul_f32 v[118:119], v[130:131], v[118:119] op_sel_hi:[0,1]
	v_pk_mul_f32 v[114:115], v[130:131], v[114:115] op_sel_hi:[0,1]
	v_lshl_add_u32 v128, v4, 10, v146
	v_med3_f32 v5, v118, s75, v164
	v_med3_f32 v118, v114, s75, v164
	v_med3_f32 v119, v119, s75, v164
	v_mov_b32_e32 v114, v147
	v_cvt_pk_fp8_f32 v114, v5, v119
	v_pk_fma_f32 v[120:121], v[120:121], s[38:39], v[156:157] op_sel_hi:[1,0,1]
	v_pk_fma_f32 v[116:117], v[116:117], s[38:39], v[152:153] op_sel_hi:[1,0,1]
	v_pk_mul_f32 v[120:121], v[130:131], v[120:121] op_sel_hi:[0,1]
	v_pk_mul_f32 v[116:117], v[130:131], v[116:117] op_sel_hi:[0,1]
	v_med3_f32 v131, v115, s75, v164
	v_pk_fma_f32 v[110:111], v[110:111], s[38:39], v[150:151] op_sel_hi:[1,0,1]
	v_pk_fma_f32 v[106:107], v[106:107], s[38:39], v[6:7] op_sel_hi:[1,0,1]
	v_med3_f32 v120, v120, s75, v164
	v_med3_f32 v5, v121, s75, v164
	v_pk_mul_f32 v[110:111], v[130:131], v[110:111] op_sel_hi:[0,1]
	v_pk_mul_f32 v[106:107], v[130:131], v[106:107] op_sel_hi:[0,1]
	v_cvt_pk_fp8_f32 v114, v120, v5 op_sel:[0,0,1]
	v_med3_f32 v5, v110, s75, v164
	v_med3_f32 v110, v106, s75, v164
	v_med3_f32 v111, v111, s75, v164
	v_mov_b32_e32 v106, v147
	v_cvt_pk_fp8_f32 v106, v5, v111
	v_pk_fma_f32 v[112:113], v[112:113], s[38:39], v[8:9] op_sel_hi:[1,0,1]
	v_mov_b32_e32 v115, v147
	v_pk_mul_f32 v[112:113], v[130:131], v[112:113] op_sel_hi:[0,1]
	v_med3_f32 v112, v112, s75, v164
	v_med3_f32 v5, v113, s75, v164
	v_cvt_pk_fp8_f32 v106, v112, v5 op_sel:[0,0,1]
	v_mul_f32_e32 v112, 0x41000000, v169
	v_pk_fma_f32 v[102:103], v[102:103], s[38:39], v[158:159] op_sel_hi:[1,0,1]
	v_pk_fma_f32 v[98:99], v[98:99], s[38:39], v[154:155] op_sel_hi:[1,0,1]
	v_cvt_pk_fp8_f32 v115, v118, v131
	v_pk_mul_f32 v[102:103], v[112:113], v[102:103] op_sel_hi:[0,1]
	v_pk_mul_f32 v[98:99], v[112:113], v[98:99] op_sel_hi:[0,1]
	v_med3_f32 v5, v102, s75, v164
	v_med3_f32 v102, v98, s75, v164
	v_med3_f32 v103, v103, s75, v164
	v_mov_b32_e32 v98, v147
	v_cvt_pk_fp8_f32 v98, v5, v103
	v_med3_f32 v116, v116, s75, v164
	v_med3_f32 v117, v117, s75, v164
	v_pk_fma_f32 v[104:105], v[104:105], s[38:39], v[156:157] op_sel_hi:[1,0,1]
	v_pk_fma_f32 v[100:101], v[100:101], s[38:39], v[152:153] op_sel_hi:[1,0,1]
	v_cvt_pk_fp8_f32 v115, v116, v117 op_sel:[0,0,1]
	v_med3_f32 v116, v107, s75, v164
	v_mov_b32_e32 v107, v147
	v_pk_mul_f32 v[104:105], v[112:113], v[104:105] op_sel_hi:[0,1]
	v_pk_mul_f32 v[100:101], v[112:113], v[100:101] op_sel_hi:[0,1]
	v_med3_f32 v113, v99, s75, v164
	v_pk_fma_f32 v[94:95], v[94:95], s[38:39], v[150:151] op_sel_hi:[1,0,1]
	v_pk_fma_f32 v[90:91], v[90:91], s[38:39], v[6:7] op_sel_hi:[1,0,1]
	v_cvt_pk_fp8_f32 v107, v110, v116
	v_med3_f32 v104, v104, s75, v164
	v_med3_f32 v5, v105, s75, v164
	v_pk_mul_f32 v[94:95], v[112:113], v[94:95] op_sel_hi:[0,1]
	v_pk_mul_f32 v[90:91], v[112:113], v[90:91] op_sel_hi:[0,1]
	v_pk_fma_f32 v[108:109], v[108:109], s[38:39], v[2:3] op_sel_hi:[1,0,1]
	v_mov_b32_e32 v99, v147
	v_cvt_pk_fp8_f32 v98, v104, v5 op_sel:[0,0,1]
	v_med3_f32 v5, v94, s75, v164
	v_med3_f32 v94, v90, s75, v164
	v_med3_f32 v95, v95, s75, v164
	v_mov_b32_e32 v90, v147
	s_lshl_b32 s8, s62, 8
	ds_read_b128 v[124:127], v123
	v_pk_mul_f32 v[108:109], v[130:131], v[108:109] op_sel_hi:[0,1]
	v_cvt_pk_fp8_f32 v99, v102, v113
	v_cvt_pk_fp8_f32 v90, v5, v95
	s_or_b32 s8, s9, s8
	v_med3_f32 v108, v108, s75, v164
	v_med3_f32 v109, v109, s75, v164
	v_pk_fma_f32 v[96:97], v[96:97], s[38:39], v[8:9] op_sel_hi:[1,0,1]
	s_ashr_i32 s9, s8, 31
	v_cvt_pk_fp8_f32 v107, v108, v109 op_sel:[0,0,1]
	v_pk_mul_f32 v[96:97], v[112:113], v[96:97] op_sel_hi:[0,1]
	s_add_u32 s86, s16, s8
	s_addc_u32 s87, s17, s9
	v_med3_f32 v100, v100, s75, v164
	v_med3_f32 v101, v101, s75, v164
	v_med3_f32 v96, v96, s75, v164
	v_med3_f32 v5, v97, s75, v164
	v_mov_b32_e32 v108, v128
	v_cvt_pk_fp8_f32 v99, v100, v101 op_sel:[0,0,1]
	v_med3_f32 v100, v91, s75, v164
	v_mov_b32_e32 v91, v147
	v_cvt_pk_fp8_f32 v90, v96, v5 op_sel:[0,0,1]
	v_mul_f32_e32 v96, 0x41000000, v168
	v_pk_fma_f32 v[78:79], v[78:79], s[38:39], v[158:159] op_sel_hi:[1,0,1]
	v_pk_fma_f32 v[74:75], v[74:75], s[38:39], v[154:155] op_sel_hi:[1,0,1]
	s_waitcnt lgkmcnt(0)
	global_store_dwordx4 v108, v[124:127], s[86:87]
	v_cvt_pk_fp8_f32 v91, v94, v100
	v_pk_fma_f32 v[80:81], v[80:81], s[38:39], v[156:157] op_sel_hi:[1,0,1]
	v_pk_mul_f32 v[78:79], v[96:97], v[78:79] op_sel_hi:[0,1]
	v_pk_fma_f32 v[76:77], v[76:77], s[38:39], v[152:153] op_sel_hi:[1,0,1]
	v_pk_mul_f32 v[74:75], v[96:97], v[74:75] op_sel_hi:[0,1]
	ds_write2_b64 v122, v[114:115], v[106:107] offset1:4
	v_or_b32_e32 v110, 16, v4
	v_pk_fma_f32 v[92:93], v[92:93], s[38:39], v[2:3] op_sel_hi:[1,0,1]
	v_pk_mul_f32 v[80:81], v[96:97], v[80:81] op_sel_hi:[0,1]
	v_pk_mul_f32 v[76:77], v[96:97], v[76:77] op_sel_hi:[0,1]
	v_med3_f32 v5, v78, s75, v164
	v_med3_f32 v78, v74, s75, v164
	v_med3_f32 v79, v79, s75, v164
	v_med3_f32 v97, v75, s75, v164
	v_mov_b32_e32 v74, v147
	v_mov_b32_e32 v75, v147
	ds_read_b128 v[106:109], v123
	v_ashrrev_i32_e32 v111, 31, v110
	v_pk_mul_f32 v[92:93], v[112:113], v[92:93] op_sel_hi:[0,1]
	v_cvt_pk_fp8_f32 v74, v5, v79
	v_cvt_pk_fp8_f32 v75, v78, v97
	v_lshl_add_u32 v110, v110, 10, v146
	v_med3_f32 v92, v92, s75, v164
	v_med3_f32 v93, v93, s75, v164
	v_cvt_pk_fp8_f32 v91, v92, v93 op_sel:[0,0,1]
	v_pk_fma_f32 v[62:63], v[62:63], s[38:39], v[150:151] op_sel_hi:[1,0,1]
	v_pk_fma_f32 v[58:59], v[58:59], s[38:39], v[6:7] op_sel_hi:[1,0,1]
	s_add_u32 s86, s16, s8
	s_addc_u32 s87, s17, s9
	v_med3_f32 v80, v80, s75, v164
	v_med3_f32 v76, v76, s75, v164
	v_med3_f32 v5, v81, s75, v164
	v_med3_f32 v77, v77, s75, v164
	v_pk_mul_f32 v[62:63], v[96:97], v[62:63] op_sel_hi:[0,1]
	v_pk_mul_f32 v[58:59], v[96:97], v[58:59] op_sel_hi:[0,1]
	v_mov_b32_e32 v92, v110
	v_cvt_pk_fp8_f32 v74, v80, v5 op_sel:[0,0,1]
	v_cvt_pk_fp8_f32 v75, v76, v77 op_sel:[0,0,1]
	v_med3_f32 v5, v62, s75, v164
	v_med3_f32 v62, v58, s75, v164
	v_med3_f32 v63, v63, s75, v164
	v_med3_f32 v76, v59, s75, v164
	v_mov_b32_e32 v58, v147
	v_mov_b32_e32 v59, v147
	s_waitcnt lgkmcnt(0)
	global_store_dwordx4 v92, v[106:109], s[86:87]
	v_cvt_pk_fp8_f32 v58, v5, v63
	v_cvt_pk_fp8_f32 v59, v62, v76
	ds_write2_b64 v122, v[98:99], v[90:91] offset1:4
	v_or_b32_e32 v94, 32, v4
	v_pk_fma_f32 v[64:65], v[64:65], s[38:39], v[8:9] op_sel_hi:[1,0,1]
	v_pk_fma_f32 v[60:61], v[60:61], s[38:39], v[2:3] op_sel_hi:[1,0,1]
	ds_read_b128 v[90:93], v123
	v_ashrrev_i32_e32 v95, 31, v94
	v_pk_mul_f32 v[64:65], v[96:97], v[64:65] op_sel_hi:[0,1]
	v_pk_mul_f32 v[60:61], v[96:97], v[60:61] op_sel_hi:[0,1]
	v_lshl_add_u32 v94, v94, 10, v146
	v_med3_f32 v64, v64, s75, v164
	v_med3_f32 v60, v60, s75, v164
	v_med3_f32 v5, v65, s75, v164
	v_med3_f32 v61, v61, s75, v164
	v_cvt_pk_fp8_f32 v58, v64, v5 op_sel:[0,0,1]
	v_cvt_pk_fp8_f32 v59, v60, v61 op_sel:[0,0,1]
	s_add_u32 s86, s16, s8
	s_addc_u32 s87, s17, s9
	v_mov_b32_e32 v60, v94
	s_waitcnt lgkmcnt(0)
	global_store_dwordx4 v60, v[90:93], s[86:87]
	ds_write2_b64 v122, v[74:75], v[58:59] offset1:4
	v_mul_f32_e32 v64, 0x41000000, v167
	v_pk_fma_f32 v[74:75], v[86:87], s[38:39], v[158:159] op_sel_hi:[1,0,1]
	v_pk_fma_f32 v[78:79], v[82:83], s[38:39], v[154:155] op_sel_hi:[1,0,1]
	v_pk_mul_f32 v[74:75], v[64:65], v[74:75] op_sel_hi:[0,1]
	v_pk_fma_f32 v[76:77], v[88:89], s[38:39], v[156:157] op_sel_hi:[1,0,1]
	v_pk_fma_f32 v[80:81], v[84:85], s[38:39], v[152:153] op_sel_hi:[1,0,1]
	v_pk_mul_f32 v[78:79], v[64:65], v[78:79] op_sel_hi:[0,1]
	v_med3_f32 v5, v74, s75, v164
	v_med3_f32 v75, v75, s75, v164
	v_mov_b32_e32 v74, v147
	v_pk_mul_f32 v[76:77], v[64:65], v[76:77] op_sel_hi:[0,1]
	v_pk_mul_f32 v[80:81], v[64:65], v[80:81] op_sel_hi:[0,1]
	v_med3_f32 v65, v78, s75, v164
	v_med3_f32 v78, v79, s75, v164
	v_cvt_pk_fp8_f32 v74, v5, v75
	v_mov_b32_e32 v75, v147
	v_cvt_pk_fp8_f32 v75, v65, v78
	v_med3_f32 v79, v80, s75, v164
	v_med3_f32 v65, v81, s75, v164
	v_pk_fma_f32 v[70:71], v[70:71], s[38:39], v[150:151] op_sel_hi:[1,0,1]
	v_pk_fma_f32 v[72:73], v[72:73], s[38:39], v[8:9] op_sel_hi:[1,0,1]
	v_pk_fma_f32 v[66:67], v[66:67], s[38:39], v[6:7] op_sel_hi:[1,0,1]
	v_pk_fma_f32 v[68:69], v[68:69], s[38:39], v[2:3] op_sel_hi:[1,0,1]
	v_med3_f32 v76, v76, s75, v164
	v_med3_f32 v5, v77, s75, v164
	v_cvt_pk_fp8_f32 v75, v79, v65 op_sel:[0,0,1]
	v_pk_mul_f32 v[72:73], v[64:65], v[72:73] op_sel_hi:[0,1]
	v_pk_mul_f32 v[70:71], v[64:65], v[70:71] op_sel_hi:[0,1]
	v_pk_mul_f32 v[68:69], v[64:65], v[68:69] op_sel_hi:[0,1]
	v_pk_mul_f32 v[64:65], v[64:65], v[66:67] op_sel_hi:[0,1]
	v_cvt_pk_fp8_f32 v74, v76, v5 op_sel:[0,0,1]
	v_med3_f32 v5, v70, s75, v164
	v_med3_f32 v66, v64, s75, v164
	v_med3_f32 v67, v71, s75, v164
	v_med3_f32 v70, v65, s75, v164
	v_mov_b32_e32 v64, v147
	v_mov_b32_e32 v65, v147
	v_cvt_pk_fp8_f32 v64, v5, v67
	v_cvt_pk_fp8_f32 v65, v66, v70
	v_or_b32_e32 v62, 48, v4
	ds_read_b128 v[58:61], v123
	v_ashrrev_i32_e32 v63, 31, v62
	v_lshl_add_u32 v62, v62, 10, v146
	v_med3_f32 v71, v72, s75, v164
	v_med3_f32 v68, v68, s75, v164
	v_med3_f32 v5, v73, s75, v164
	v_med3_f32 v66, v69, s75, v164
	v_cvt_pk_fp8_f32 v64, v71, v5 op_sel:[0,0,1]
	v_cvt_pk_fp8_f32 v65, v68, v66 op_sel:[0,0,1]
	s_add_u32 s86, s16, s8
	s_addc_u32 s87, s17, s9
	s_waitcnt lgkmcnt(0)
	global_store_dwordx4 v62, v[58:61], s[86:87]
	ds_write2_b64 v122, v[74:75], v[64:65] offset1:4
	v_mul_f32_e32 v64, 0x41000000, v166
	v_pk_fma_f32 v[54:55], v[54:55], s[38:39], v[158:159] op_sel_hi:[1,0,1]
	v_pk_fma_f32 v[50:51], v[50:51], s[38:39], v[154:155] op_sel_hi:[1,0,1]
	v_pk_mul_f32 v[54:55], v[64:65], v[54:55] op_sel_hi:[0,1]
	v_pk_mul_f32 v[50:51], v[64:65], v[50:51] op_sel_hi:[0,1]
	v_med3_f32 v5, v54, s75, v164
	v_med3_f32 v54, v50, s75, v164
	v_med3_f32 v55, v55, s75, v164
	v_mov_b32_e32 v50, v147
	v_cvt_pk_fp8_f32 v50, v5, v55
	v_pk_fma_f32 v[56:57], v[56:57], s[38:39], v[156:157] op_sel_hi:[1,0,1]
	v_pk_fma_f32 v[52:53], v[52:53], s[38:39], v[152:153] op_sel_hi:[1,0,1]
	v_pk_mul_f32 v[56:57], v[64:65], v[56:57] op_sel_hi:[0,1]
	v_pk_mul_f32 v[52:53], v[64:65], v[52:53] op_sel_hi:[0,1]
	v_med3_f32 v65, v51, s75, v164
	v_pk_fma_f32 v[46:47], v[46:47], s[38:39], v[150:151] op_sel_hi:[1,0,1]
	v_pk_fma_f32 v[42:43], v[42:43], s[38:39], v[6:7] op_sel_hi:[1,0,1]
	v_med3_f32 v56, v56, s75, v164
	v_med3_f32 v5, v57, s75, v164
	v_pk_mul_f32 v[46:47], v[64:65], v[46:47] op_sel_hi:[0,1]
	v_pk_mul_f32 v[42:43], v[64:65], v[42:43] op_sel_hi:[0,1]
	v_cvt_pk_fp8_f32 v50, v56, v5 op_sel:[0,0,1]
	v_med3_f32 v5, v46, s75, v164
	v_med3_f32 v46, v42, s75, v164
	v_med3_f32 v47, v47, s75, v164
	v_mov_b32_e32 v42, v147
	v_cvt_pk_fp8_f32 v42, v5, v47
	v_pk_fma_f32 v[48:49], v[48:49], s[38:39], v[8:9] op_sel_hi:[1,0,1]
	v_mov_b32_e32 v51, v147
	v_pk_mul_f32 v[48:49], v[64:65], v[48:49] op_sel_hi:[0,1]
	v_med3_f32 v48, v48, s75, v164
	v_med3_f32 v5, v49, s75, v164
	v_cvt_pk_fp8_f32 v42, v48, v5 op_sel:[0,0,1]
	v_mul_f32_e32 v48, 0x41000000, v165
	v_pk_fma_f32 v[38:39], v[38:39], s[38:39], v[158:159] op_sel_hi:[1,0,1]
	v_pk_fma_f32 v[34:35], v[34:35], s[38:39], v[154:155] op_sel_hi:[1,0,1]
	v_cvt_pk_fp8_f32 v51, v54, v65
	v_pk_mul_f32 v[38:39], v[48:49], v[38:39] op_sel_hi:[0,1]
	v_pk_mul_f32 v[34:35], v[48:49], v[34:35] op_sel_hi:[0,1]
	v_med3_f32 v5, v38, s75, v164
	v_med3_f32 v38, v34, s75, v164
	v_med3_f32 v39, v39, s75, v164
	v_mov_b32_e32 v34, v147
	v_cvt_pk_fp8_f32 v34, v5, v39
	v_med3_f32 v52, v52, s75, v164
	v_med3_f32 v53, v53, s75, v164
	v_pk_fma_f32 v[40:41], v[40:41], s[38:39], v[156:157] op_sel_hi:[1,0,1]
	v_pk_fma_f32 v[36:37], v[36:37], s[38:39], v[152:153] op_sel_hi:[1,0,1]
	v_cvt_pk_fp8_f32 v51, v52, v53 op_sel:[0,0,1]
	v_med3_f32 v52, v43, s75, v164
	v_mov_b32_e32 v43, v147
	v_pk_mul_f32 v[40:41], v[48:49], v[40:41] op_sel_hi:[0,1]
	v_pk_mul_f32 v[36:37], v[48:49], v[36:37] op_sel_hi:[0,1]
	v_med3_f32 v49, v35, s75, v164
	v_pk_fma_f32 v[30:31], v[30:31], s[38:39], v[150:151] op_sel_hi:[1,0,1]
	v_pk_fma_f32 v[26:27], v[26:27], s[38:39], v[6:7] op_sel_hi:[1,0,1]
	v_cvt_pk_fp8_f32 v43, v46, v52
	v_med3_f32 v40, v40, s75, v164
	v_med3_f32 v5, v41, s75, v164
	v_pk_mul_f32 v[30:31], v[48:49], v[30:31] op_sel_hi:[0,1]
	v_pk_mul_f32 v[26:27], v[48:49], v[26:27] op_sel_hi:[0,1]
	v_add_u32_e32 v62, 0x80, v4
	v_pk_fma_f32 v[44:45], v[44:45], s[38:39], v[2:3] op_sel_hi:[1,0,1]
	v_mov_b32_e32 v35, v147
	v_cvt_pk_fp8_f32 v34, v40, v5 op_sel:[0,0,1]
	v_med3_f32 v5, v30, s75, v164
	v_med3_f32 v30, v26, s75, v164
	v_med3_f32 v31, v31, s75, v164
	v_mov_b32_e32 v26, v147
	ds_read_b128 v[58:61], v123
	v_ashrrev_i32_e32 v63, 31, v62
	v_pk_mul_f32 v[44:45], v[64:65], v[44:45] op_sel_hi:[0,1]
	v_cvt_pk_fp8_f32 v35, v38, v49
	v_cvt_pk_fp8_f32 v26, v5, v31
	v_lshl_add_u32 v62, v62, 10, v146
	v_med3_f32 v44, v44, s75, v164
	v_med3_f32 v45, v45, s75, v164
	v_pk_fma_f32 v[32:33], v[32:33], s[38:39], v[8:9] op_sel_hi:[1,0,1]
	v_cvt_pk_fp8_f32 v43, v44, v45 op_sel:[0,0,1]
	v_pk_mul_f32 v[32:33], v[48:49], v[32:33] op_sel_hi:[0,1]
	s_add_u32 s86, s16, s8
	s_addc_u32 s87, s17, s9
	v_med3_f32 v36, v36, s75, v164
	v_med3_f32 v37, v37, s75, v164
	v_med3_f32 v32, v32, s75, v164
	v_med3_f32 v5, v33, s75, v164
	v_mov_b32_e32 v44, v62
	v_cvt_pk_fp8_f32 v35, v36, v37 op_sel:[0,0,1]
	v_med3_f32 v36, v27, s75, v164
	v_mov_b32_e32 v27, v147
	v_cvt_pk_fp8_f32 v26, v32, v5 op_sel:[0,0,1]
	v_mul_f32_e32 v32, 0x41000000, v1
	v_pk_fma_f32 v[22:23], v[22:23], s[38:39], v[158:159] op_sel_hi:[1,0,1]
	v_pk_fma_f32 v[18:19], v[18:19], s[38:39], v[154:155] op_sel_hi:[1,0,1]
	s_waitcnt lgkmcnt(0)
	global_store_dwordx4 v44, v[58:61], s[86:87]
	v_cvt_pk_fp8_f32 v27, v30, v36
	v_pk_mul_f32 v[22:23], v[32:33], v[22:23] op_sel_hi:[0,1]
	v_pk_mul_f32 v[18:19], v[32:33], v[18:19] op_sel_hi:[0,1]
	ds_write2_b64 v122, v[50:51], v[42:43] offset1:4
	v_add_u32_e32 v46, 0x90, v4
	v_pk_fma_f32 v[28:29], v[28:29], s[38:39], v[2:3] op_sel_hi:[1,0,1]
	v_med3_f32 v1, v22, s75, v164
	v_med3_f32 v5, v18, s75, v164
	v_med3_f32 v22, v23, s75, v164
	v_med3_f32 v23, v19, s75, v164
	v_mov_b32_e32 v18, v147
	v_mov_b32_e32 v19, v147
	ds_read_b128 v[42:45], v123
	v_ashrrev_i32_e32 v47, 31, v46
	v_pk_mul_f32 v[28:29], v[48:49], v[28:29] op_sel_hi:[0,1]
	v_cvt_pk_fp8_f32 v18, v1, v22
	v_cvt_pk_fp8_f32 v19, v5, v23
	v_lshl_add_u32 v46, v46, 10, v146
	v_med3_f32 v28, v28, s75, v164
	v_med3_f32 v29, v29, s75, v164
	v_pk_fma_f32 v[24:25], v[24:25], s[38:39], v[156:157] op_sel_hi:[1,0,1]
	v_pk_fma_f32 v[20:21], v[20:21], s[38:39], v[152:153] op_sel_hi:[1,0,1]
	v_cvt_pk_fp8_f32 v27, v28, v29 op_sel:[0,0,1]
	v_pk_mul_f32 v[24:25], v[32:33], v[24:25] op_sel_hi:[0,1]
	v_pk_mul_f32 v[20:21], v[32:33], v[20:21] op_sel_hi:[0,1]
	v_pk_fma_f32 v[14:15], v[14:15], s[38:39], v[150:151] op_sel_hi:[1,0,1]
	v_pk_fma_f32 v[6:7], v[10:11], s[38:39], v[6:7] op_sel_hi:[1,0,1]
	s_add_u32 s86, s16, s8
	s_addc_u32 s87, s17, s9
	v_med3_f32 v24, v24, s75, v164
	v_med3_f32 v20, v20, s75, v164
	v_med3_f32 v1, v25, s75, v164
	v_med3_f32 v5, v21, s75, v164
	v_pk_mul_f32 v[14:15], v[32:33], v[14:15] op_sel_hi:[0,1]
	v_pk_mul_f32 v[6:7], v[32:33], v[6:7] op_sel_hi:[0,1]
	v_mov_b32_e32 v28, v46
	v_cvt_pk_fp8_f32 v18, v24, v1 op_sel:[0,0,1]
	v_cvt_pk_fp8_f32 v19, v20, v5 op_sel:[0,0,1]
	v_med3_f32 v1, v14, s75, v164
	v_med3_f32 v5, v6, s75, v164
	v_med3_f32 v10, v15, s75, v164
	v_med3_f32 v11, v7, s75, v164
	v_mov_b32_e32 v6, v147
	v_mov_b32_e32 v7, v147
	s_waitcnt lgkmcnt(0)
	global_store_dwordx4 v28, v[42:45], s[86:87]
	v_cvt_pk_fp8_f32 v6, v1, v10
	v_cvt_pk_fp8_f32 v7, v5, v11
	ds_write2_b64 v122, v[34:35], v[26:27] offset1:4
	v_add_u32_e32 v30, 0xa0, v4
	v_pk_fma_f32 v[8:9], v[16:17], s[38:39], v[8:9] op_sel_hi:[1,0,1]
	v_pk_fma_f32 v[2:3], v[12:13], s[38:39], v[2:3] op_sel_hi:[1,0,1]
	ds_read_b128 v[26:29], v123
	v_ashrrev_i32_e32 v31, 31, v30
	v_pk_mul_f32 v[8:9], v[32:33], v[8:9] op_sel_hi:[0,1]
	v_pk_mul_f32 v[2:3], v[32:33], v[2:3] op_sel_hi:[0,1]
	v_lshl_add_u32 v30, v30, 10, v146
	v_med3_f32 v8, v8, s75, v164
	v_med3_f32 v2, v2, s75, v164
	v_med3_f32 v1, v9, s75, v164
	v_med3_f32 v3, v3, s75, v164
	v_cvt_pk_fp8_f32 v6, v8, v1 op_sel:[0,0,1]
	v_cvt_pk_fp8_f32 v7, v2, v3 op_sel:[0,0,1]
	s_add_u32 s86, s16, s8
	s_addc_u32 s87, s17, s9
	v_mov_b32_e32 v2, v30
	s_waitcnt lgkmcnt(0)
	global_store_dwordx4 v2, v[26:29], s[86:87]
	ds_write2_b64 v122, v[18:19], v[6:7] offset1:4
	v_add_u32_e32 v2, 0xb0, v4
	ds_read_b128 v[6:9], v123
	v_ashrrev_i32_e32 v3, 31, v2
	v_lshl_add_u32 v2, v2, 10, v146
	s_add_u32 s86, s16, s8
	s_addc_u32 s87, s17, s9
	s_waitcnt lgkmcnt(0)
	global_store_dwordx4 v2, v[6:9], s[86:87]
	s_and_b64 vcc, exec, s[10:11]
	s_mov_b64 s[8:9], -1
	s_cbranch_vccnz .LBB0_3418
	v_mov_b32_e32 v12, v0
	s_lshl_b32 s9, s42, 8
	v_readfirstlane_b32 s8, v12
	s_and_b32 s10, s8, 0xc0
	s_ashr_i32 s8, s8, 2
	s_andn2_b32 s8, s8, 63
	s_add_i32 s8, s8, s9
	v_and_or_b32 v2, v12, 15, s8
	v_lshlrev_b32_e32 v4, 2, v2
	s_lshl_b64 s[8:9], s[44:45], 11
	s_add_u32 s11, s54, s8
	s_addc_u32 s41, s55, s9
	s_lshl_b32 s8, s40, 8
	global_load_dword v146, v4, s[12:13] offset:0
	global_load_dword v170, v4, s[12:13] offset:64
	global_load_dword v169, v4, s[12:13] offset:128
	global_load_dword v168, v4, s[12:13] offset:192
	global_load_dword v167, v4, s[12:13] offset:512
	global_load_dword v166, v4, s[12:13] offset:576
	global_load_dword v165, v4, s[12:13] offset:640
	global_load_dword v1, v4, s[12:13] offset:704
	s_ashr_i32 s9, s8, 31
	s_lshl_b64 s[8:9], s[8:9], 1
	s_add_u32 s8, s11, s8
	s_addc_u32 s9, s41, s9
	s_lshl_b32 s10, s10, 1
	s_add_u32 s8, s8, s10
	s_addc_u32 s9, s9, 0
	v_and_b32_e32 v2, 48, v12
	global_load_dwordx4 v[6:9], v2, s[8:9]
	s_nop 0
	global_load_dwordx4 v[2:5], v2, s[8:9] offset:64
	s_andn2_b64 vcc, exec, s[14:15]
	s_cbranch_vccnz .LBB0_3417
	s_barrier
	s_branch .LBB0_3417
